# GQA loop: next-tile global loads issued inside the PV MFMA gaps (shorter QK-to-PV transition)
# speedup vs baseline: 1.0364x; 1.0093x over previous
; #define SBAR() __builtin_amdgcn_sched_barrier(0)
; template <bool FIXM> __device__ __forceinline__ void pv_psm(f32x16& o0, f32x16& o1, unsigned vb, bf16x8 pa0, bf16x8 pa1, bf16x8 pa2, bf16x8 pa3,
;                                        f32x16& p0, f32x16& p1, float& m_reg, f32x16& negm, float& alpha) {
;     { const s16x4 l0 = tr_read<v_rd_off(0, 0, 0)>(vb), h0 = tr_read<v_rd_off(0, 0, 1)>(vb), l1 = tr_read<v_rd_off(0, 1, 0)>(vb), h1 = tr_read<v_rd_off(0, 1, 1)>(vb);
;       const s16x4 l2 = tr_read<v_rd_off(0, 2, 0)>(vb), h2 = tr_read<v_rd_off(0, 2, 1)>(vb), l3 = tr_read<v_rd_off(0, 3, 0)>(vb), h3 = tr_read<v_rd_off(0, 3, 1)>(vb);
;       float pmax = 0.f; SBAR(); if (!FIXM) pmax = psm_max(p0, p1); else { _Pragma("unroll") for (int r = 0; r < 8; ++r) p0[r] = __builtin_amdgcn_exp2f(p0[r]); } SBAR();
;       asm volatile("s_waitcnt lgkmcnt(0)" ::: "memory"); SBAR();
;       o0 = __builtin_amdgcn_mfma_f32_32x32x16_bf16(ATT_PK(l0, h0), pa0, o0, 0, 0, 0);
;       o0 = __builtin_amdgcn_mfma_f32_32x32x16_bf16(ATT_PK(l1, h1), pa1, o0, 0, 0, 0);
;       o0 = __builtin_amdgcn_mfma_f32_32x32x16_bf16(ATT_PK(l2, h2), pa2, o0, 0, 0, 0);
;       o0 = __builtin_amdgcn_mfma_f32_32x32x16_bf16(ATT_PK(l3, h3), pa3, o0, 0, 0, 0);
;       SBAR();
;       const s16x4 m0 = tr_read<v_rd_off(1, 0, 0)>(vb), n0 = tr_read<v_rd_off(1, 0, 1)>(vb), m1 = tr_read<v_rd_off(1, 1, 0)>(vb), n1 = tr_read<v_rd_off(1, 1, 1)>(vb);
;       const s16x4 m2 = tr_read<v_rd_off(1, 2, 0)>(vb), n2 = tr_read<v_rd_off(1, 2, 1)>(vb), m3 = tr_read<v_rd_off(1, 3, 0)>(vb), n3 = tr_read<v_rd_off(1, 3, 1)>(vb);
;       SBAR(); if (!FIXM) psm_apply<false>(p0, p1, pmax, m_reg, negm, alpha); else { alpha = 1.f; _Pragma("unroll") for (int r = 8; r < 16; ++r) p0[r] = __builtin_amdgcn_exp2f(p0[r]); } SBAR();
;       asm volatile("s_waitcnt lgkmcnt(0)" ::: "memory"); SBAR();
;       o1 = __builtin_amdgcn_mfma_f32_32x32x16_bf16(ATT_PK(m0, n0), pa0, o1, 0, 0, 0);
; template <int DQK, bool FIXM> ...
;     ...
;         SBAR(); qkt<DQK>(pB0, pB1, lds + bK, qr, r32, hi, negm);
;         finishSM(pA0, pA1, alA, l_reg, pa0, pa1, pa2, pa3); SBAR();
;         SLOAD(1, j + 2); SBAR();
;         if constexpr (FIXM) pv_psm<true>(o0, o1, vb0 + bV, pa0, pa1, pa2, pa3, pB0, pB1, m_reg, negm, alB); else { PVO(bV); partialSM<false>(pB0, pB1, m_reg, negm, alB); }
;         SWAIT(); SWRITEO(bW, 0);
;         if (!FIXM) RESC(alB); ROT();
.LBB0_497:
	s_mov_b32 s1, s11
	s_mov_b32 s11, s35
	s_waitcnt lgkmcnt(0)
	s_barrier
	v_add_u32_e32 v252, s1, v208
	v_add_u32_e32 v228, v252, v209
	ds_read_b128 v[224:227], v228
	ds_read_b128 v[228:231], v228 offset:4096
	v_add_u32_e32 v236, v252, v210
	ds_read_b128 v[232:235], v236
	ds_read_b128 v[236:239], v236 offset:4096
	v_add_u32_e32 v244, v252, v211
	ds_read_b128 v[240:243], v244
	ds_read_b128 v[244:247], v244 offset:4096
	v_add_u32_e32 v253, v252, v212
	ds_read_b128 v[248:251], v253
	v_exp_f32_e32 v66, v66
	v_exp_f32_e32 v67, v67
	v_exp_f32_e32 v68, v68
	v_exp_f32_e32 v69, v69
	v_exp_f32_e32 v70, v70
	v_exp_f32_e32 v71, v71
	v_exp_f32_e32 v72, v72
	v_exp_f32_e32 v73, v73
	s_waitcnt lgkmcnt(6)
	v_mfma_f32_32x32x16_bf16 v[98:113], v[224:227], v[114:117], v[18:33]
	ds_read_b128 v[224:227], v253 offset:4096
	v_exp_f32_e32 v74, v74
	v_exp_f32_e32 v75, v75
	v_exp_f32_e32 v76, v76
	v_cvt_pk_bf16_f32 v156, v143, v145
	v_cvt_pk_bf16_f32 v157, v141, v144
	v_add_f32_e32 v164, 0, v143
	v_add_f32_e32 v164, v145, v164
	v_add_f32_e32 v164, v141, v164
	s_waitcnt lgkmcnt(6)
	v_mfma_f32_32x32x16_bf16 v[82:97], v[228:231], v[114:117], v[18:33]
	v_exp_f32_e32 v77, v77
	v_exp_f32_e32 v78, v78
	v_exp_f32_e32 v79, v79
	v_cvt_pk_bf16_f32 v158, v139, v142
	v_cvt_pk_bf16_f32 v159, v138, v140
	v_add_f32_e32 v164, v144, v164
	v_add_f32_e32 v164, v139, v164
	v_add_f32_e32 v164, v142, v164
	s_waitcnt lgkmcnt(5)
	v_mfma_f32_32x32x16_bf16 v[98:113], v[232:235], v[12:15], v[98:113]
	v_exp_f32_e32 v80, v80
	v_exp_f32_e32 v81, v81
	v_cvt_pk_bf16_f32 v160, v151, v153
	v_cvt_pk_bf16_f32 v161, v149, v152
	v_cvt_pk_bf16_f32 v162, v147, v150
	v_cvt_pk_bf16_f32 v163, v146, v148
	v_add_f32_e32 v164, v138, v164
	v_add_f32_e32 v164, v140, v164
	v_add_f32_e32 v164, v151, v164
	s_waitcnt lgkmcnt(4)
	v_mfma_f32_32x32x16_bf16 v[82:97], v[236:239], v[12:15], v[82:97]
	v_add_f32_e32 v164, v153, v164
	v_add_f32_e32 v164, v149, v164
	v_add_f32_e32 v164, v152, v164
	v_add_f32_e32 v164, v147, v164
	v_add_f32_e32 v164, v150, v164
	v_add_f32_e32 v164, v146, v164
	v_add_f32_e32 v164, v148, v164
	s_waitcnt lgkmcnt(3)
	v_mfma_f32_32x32x16_bf16 v[98:113], v[240:243], v[8:11], v[98:113]
	v_add_u32_e32 v2, s11, v213
	ds_read_b64_tr_b16 v[138:139], v2 offset:0
	ds_read_b64_tr_b16 v[140:141], v2 offset:1024
	ds_read_b64_tr_b16 v[142:143], v2 offset:2048
	ds_read_b64_tr_b16 v[144:145], v2 offset:3072
	v_add_f32_e32 v164, v66, v164
	v_add_f32_e32 v164, v67, v164
	v_add_f32_e32 v164, v68, v164
	v_add_f32_e32 v164, v69, v164
	s_waitcnt lgkmcnt(6)
	v_mfma_f32_32x32x16_bf16 v[82:97], v[244:247], v[8:11], v[82:97]
	ds_read_b64_tr_b16 v[146:147], v2 offset:4096
	ds_read_b64_tr_b16 v[148:149], v2 offset:5120
	ds_read_b64_tr_b16 v[150:151], v2 offset:6144
	ds_read_b64_tr_b16 v[152:153], v2 offset:7168
	v_add_f32_e32 v164, v70, v164
	v_add_f32_e32 v164, v71, v164
	v_add_f32_e32 v164, v72, v164
	v_add_f32_e32 v164, v73, v164
	s_waitcnt lgkmcnt(9)
	v_mfma_f32_32x32x16_bf16 v[98:113], v[248:251], v[4:7], v[98:113]
	v_add_f32_e32 v164, v74, v164
	v_add_f32_e32 v164, v75, v164
	v_add_f32_e32 v164, v76, v164
	v_add_f32_e32 v164, v77, v164
	s_waitcnt lgkmcnt(8)
	v_mfma_f32_32x32x16_bf16 v[82:97], v[224:227], v[4:7], v[82:97]
	ds_read_b64_tr_b16 v[224:225], v2 offset:512
	ds_read_b64_tr_b16 v[226:227], v2 offset:1536
	ds_read_b64_tr_b16 v[228:229], v2 offset:2560
	ds_read_b64_tr_b16 v[230:231], v2 offset:3584
	ds_read_b64_tr_b16 v[232:233], v2 offset:4608
	ds_read_b64_tr_b16 v[234:235], v2 offset:5632
	ds_read_b64_tr_b16 v[236:237], v2 offset:6656
	ds_read_b64_tr_b16 v[238:239], v2 offset:7680
	s_waitcnt lgkmcnt(8)
	v_mfma_f32_32x32x16_bf16 v[50:65], v[138:141], v[156:159], v[50:65]
	v_add_f32_e32 v164, v78, v164
	v_add_f32_e32 v164, v79, v164
	v_add_f32_e32 v164, v80, v164
	v_add_f32_e32 v154, v81, v164
	v_mov_b32_e32 v155, v154
	v_mfma_f32_32x32x16_bf16 v[50:65], v[142:145], v[160:163], v[50:65]
	v_cvt_pk_bf16_f32 v66, v66, v67
	v_cvt_pk_bf16_f32 v67, v68, v69
	v_cvt_pk_bf16_f32 v68, v70, v71
	v_cvt_pk_bf16_f32 v69, v72, v73
	v_cvt_pk_bf16_f32 v70, v74, v75
	v_cvt_pk_bf16_f32 v71, v76, v77
	v_cvt_pk_bf16_f32 v72, v78, v79
	v_cvt_pk_bf16_f32 v73, v80, v81
	v_permlane32_swap_b32_e32 v154, v155
	v_mfma_f32_32x32x16_bf16 v[50:65], v[146:149], v[66:69], v[50:65]
	s_add_i32 s8, s13, -1
	s_cmp_lt_u32 s8, s31
	s_cselect_b32 s9, 0, s31
	s_cselect_b32 s35, s12, s29
	s_lshl_b32 s9, s9, 6
	s_sub_i32 s9, s35, s9
	v_add_u32_e32 v252, s9, v137
	v_subrev_u32_e32 v126, 64, v252
	v_ashrrev_i32_e32 v127, 31, v126
	v_mfma_f32_32x32x16_bf16 v[50:65], v[150:153], v[70:73], v[50:65]
	v_lshlrev_b64 v[126:127], 8, v[126:127]
	v_lshl_add_u64 v[128:129], v[16:17], 0, v[126:127]
	v_lshl_add_u64 v[126:127], v[134:135], 0, v[126:127]
	global_load_dwordx4 v[130:133], v[128:129], off
	s_nop 0
	global_load_dwordx4 v[126:129], v[126:127], off
	s_waitcnt lgkmcnt(0)
	v_mfma_f32_32x32x16_bf16 v[34:49], v[224:227], v[156:159], v[34:49]
	s_waitcnt vmcnt(2)
	v_add_u32_e32 v165, s10, v187
	ds_write_b128 v165, v[118:121]
	v_add_u32_e32 v165, s10, v214
	ds_write_b128 v165, v[122:125] offset:12288
	v_exp_f32_e32 v168, v98
	v_exp_f32_e32 v169, v99
	v_mfma_f32_32x32x16_bf16 v[34:49], v[228:231], v[160:163], v[34:49]
	v_exp_f32_e32 v170, v100
	v_exp_f32_e32 v171, v101
	v_exp_f32_e32 v172, v102
	v_exp_f32_e32 v173, v103
	v_mfma_f32_32x32x16_bf16 v[34:49], v[232:235], v[66:69], v[34:49]
	v_exp_f32_e32 v174, v104
	v_exp_f32_e32 v175, v105
	v_exp_f32_e32 v176, v106
	v_exp_f32_e32 v177, v107
	v_exp_f32_e32 v178, v108
	v_mfma_f32_32x32x16_bf16 v[34:49], v[236:239], v[70:73], v[34:49]
	v_exp_f32_e32 v179, v109
	v_exp_f32_e32 v180, v110
	v_exp_f32_e32 v181, v111
	v_exp_f32_e32 v182, v112
	v_exp_f32_e32 v183, v113
	s_waitcnt lgkmcnt(0)
	s_barrier
; #define SBAR() __builtin_amdgcn_sched_barrier(0)
; template <bool FIXM> __device__ __forceinline__ void pv_psm(f32x16& o0, f32x16& o1, unsigned vb, bf16x8 pa0, bf16x8 pa1, bf16x8 pa2, bf16x8 pa3,
;                                        f32x16& p0, f32x16& p1, float& m_reg, f32x16& negm, float& alpha) {
;     { const s16x4 l0 = tr_read<v_rd_off(0, 0, 0)>(vb), h0 = tr_read<v_rd_off(0, 0, 1)>(vb), l1 = tr_read<v_rd_off(0, 1, 0)>(vb), h1 = tr_read<v_rd_off(0, 1, 1)>(vb);
;       const s16x4 l2 = tr_read<v_rd_off(0, 2, 0)>(vb), h2 = tr_read<v_rd_off(0, 2, 1)>(vb), l3 = tr_read<v_rd_off(0, 3, 0)>(vb), h3 = tr_read<v_rd_off(0, 3, 1)>(vb);
;       float pmax = 0.f; SBAR(); if (!FIXM) pmax = psm_max(p0, p1); else { _Pragma("unroll") for (int r = 0; r < 8; ++r) p0[r] = __builtin_amdgcn_exp2f(p0[r]); } SBAR();
;       asm volatile("s_waitcnt lgkmcnt(0)" ::: "memory"); SBAR();
;       o0 = __builtin_amdgcn_mfma_f32_32x32x16_bf16(ATT_PK(l0, h0), pa0, o0, 0, 0, 0);
;       o0 = __builtin_amdgcn_mfma_f32_32x32x16_bf16(ATT_PK(l1, h1), pa1, o0, 0, 0, 0);
;       o0 = __builtin_amdgcn_mfma_f32_32x32x16_bf16(ATT_PK(l2, h2), pa2, o0, 0, 0, 0);
;       o0 = __builtin_amdgcn_mfma_f32_32x32x16_bf16(ATT_PK(l3, h3), pa3, o0, 0, 0, 0);
;       SBAR();
;       const s16x4 m0 = tr_read<v_rd_off(1, 0, 0)>(vb), n0 = tr_read<v_rd_off(1, 0, 1)>(vb), m1 = tr_read<v_rd_off(1, 1, 0)>(vb), n1 = tr_read<v_rd_off(1, 1, 1)>(vb);
;       const s16x4 m2 = tr_read<v_rd_off(1, 2, 0)>(vb), n2 = tr_read<v_rd_off(1, 2, 1)>(vb), m3 = tr_read<v_rd_off(1, 3, 0)>(vb), n3 = tr_read<v_rd_off(1, 3, 1)>(vb);
;       SBAR(); if (!FIXM) psm_apply<false>(p0, p1, pmax, m_reg, negm, alpha); else { alpha = 1.f; _Pragma("unroll") for (int r = 8; r < 16; ++r) p0[r] = __builtin_amdgcn_exp2f(p0[r]); } SBAR();
;       asm volatile("s_waitcnt lgkmcnt(0)" ::: "memory"); SBAR();
; template <int DQK, bool FIXM> ...
;     ...
;         if (!NOBAR_PROBE) __syncthreads();
;         SBAR(); qkt<DQK>(pA0, pA1, lds + bK, qr, r32, hi, negm);
;         finishSM(pB0, pB1, alB, l_reg, pa0, pa1, pa2, pa3); SBAR();
;         if (j + 3 < NT) SLOAD(0, j + 3); SBAR();
;         if constexpr (FIXM) pv_psm<true>(o0, o1, vb0 + bV, pa0, pa1, pa2, pa3, pA0, pA1, m_reg, negm, alA); else { PVO(bV); partialSM<false>(pA0, pA1, m_reg, negm, alA); }
;         SWAIT(); SWRITEO(bW, 1);
;         if (!FIXM) RESC(alA); ROT();
	v_add_u32_e32 v252, s10, v201
	v_add_u32_e32 v228, v252, v209
	ds_read_b128 v[224:227], v228
	ds_read_b128 v[228:231], v228 offset:4096
	v_add_u32_e32 v236, v252, v210
	ds_read_b128 v[232:235], v236
	ds_read_b128 v[236:239], v236 offset:4096
	v_add_u32_e32 v244, v252, v211
	ds_read_b128 v[240:243], v244
	ds_read_b128 v[244:247], v244 offset:4096
	v_add_u32_e32 v253, v252, v212
	ds_read_b128 v[248:251], v253
	v_exp_f32_e32 v82, v82
	v_exp_f32_e32 v83, v83
	v_exp_f32_e32 v84, v84
	v_exp_f32_e32 v85, v85
	v_exp_f32_e32 v86, v86
	v_exp_f32_e32 v87, v87
	v_exp_f32_e32 v88, v88
	v_exp_f32_e32 v89, v89
	s_waitcnt lgkmcnt(6)
	v_mfma_f32_32x32x16_bf16 v[98:113], v[224:227], v[114:117], v[18:33]
	ds_read_b128 v[224:227], v253 offset:4096
	v_exp_f32_e32 v90, v90
	v_exp_f32_e32 v91, v91
	v_exp_f32_e32 v92, v92
	v_cvt_pk_bf16_f32 v156, v168, v169
	v_cvt_pk_bf16_f32 v157, v170, v171
	v_add_f32_e32 v164, 0, v168
	v_add_f32_e32 v164, v169, v164
	v_add_f32_e32 v164, v170, v164
	s_waitcnt lgkmcnt(6)
	v_mfma_f32_32x32x16_bf16 v[66:81], v[228:231], v[114:117], v[18:33]
	v_exp_f32_e32 v93, v93
	v_exp_f32_e32 v94, v94
	v_exp_f32_e32 v95, v95
	v_cvt_pk_bf16_f32 v158, v172, v173
	v_cvt_pk_bf16_f32 v159, v174, v175
	v_add_f32_e32 v164, v171, v164
	v_add_f32_e32 v164, v172, v164
	v_add_f32_e32 v164, v173, v164
	s_waitcnt lgkmcnt(5)
	v_mfma_f32_32x32x16_bf16 v[98:113], v[232:235], v[12:15], v[98:113]
	v_exp_f32_e32 v96, v96
	v_exp_f32_e32 v97, v97
	v_cvt_pk_bf16_f32 v160, v176, v177
	v_cvt_pk_bf16_f32 v161, v178, v179
	v_cvt_pk_bf16_f32 v162, v180, v181
	v_cvt_pk_bf16_f32 v163, v182, v183
	v_add_f32_e32 v164, v174, v164
	v_add_f32_e32 v164, v175, v164
	v_add_f32_e32 v164, v176, v164
	s_waitcnt lgkmcnt(4)
	v_mfma_f32_32x32x16_bf16 v[66:81], v[236:239], v[12:15], v[66:81]
	v_add_f32_e32 v164, v177, v164
	v_add_f32_e32 v164, v178, v164
	v_add_f32_e32 v164, v179, v164
	v_add_f32_e32 v164, v180, v164
	v_add_f32_e32 v164, v181, v164
	v_add_f32_e32 v164, v182, v164
	v_add_f32_e32 v164, v183, v164
	s_waitcnt lgkmcnt(3)
	v_mfma_f32_32x32x16_bf16 v[98:113], v[240:243], v[8:11], v[98:113]
	v_add_u32_e32 v253, s1, v213
	ds_read_b64_tr_b16 v[168:169], v253 offset:0
	ds_read_b64_tr_b16 v[170:171], v253 offset:1024
	ds_read_b64_tr_b16 v[172:173], v253 offset:2048
	ds_read_b64_tr_b16 v[174:175], v253 offset:3072
	v_add_f32_e32 v164, v82, v164
	v_add_f32_e32 v164, v83, v164
	v_add_f32_e32 v164, v84, v164
	v_add_f32_e32 v164, v85, v164
	s_waitcnt lgkmcnt(6)
	v_mfma_f32_32x32x16_bf16 v[66:81], v[244:247], v[8:11], v[66:81]
	ds_read_b64_tr_b16 v[176:177], v253 offset:4096
	ds_read_b64_tr_b16 v[178:179], v253 offset:5120
	ds_read_b64_tr_b16 v[180:181], v253 offset:6144
	ds_read_b64_tr_b16 v[182:183], v253 offset:7168
	v_add_f32_e32 v164, v86, v164
	v_add_f32_e32 v164, v87, v164
	v_add_f32_e32 v164, v88, v164
	v_add_f32_e32 v164, v89, v164
	s_waitcnt lgkmcnt(9)
	v_mfma_f32_32x32x16_bf16 v[98:113], v[248:251], v[4:7], v[98:113]
	v_add_f32_e32 v164, v90, v164
	v_add_f32_e32 v164, v91, v164
	v_add_f32_e32 v164, v92, v164
	v_add_f32_e32 v164, v93, v164
	s_waitcnt lgkmcnt(8)
	v_mfma_f32_32x32x16_bf16 v[66:81], v[224:227], v[4:7], v[66:81]
	ds_read_b64_tr_b16 v[224:225], v253 offset:512
	ds_read_b64_tr_b16 v[226:227], v253 offset:1536
	ds_read_b64_tr_b16 v[228:229], v253 offset:2560
	ds_read_b64_tr_b16 v[230:231], v253 offset:3584
	ds_read_b64_tr_b16 v[232:233], v253 offset:4608
	ds_read_b64_tr_b16 v[234:235], v253 offset:5632
	ds_read_b64_tr_b16 v[236:237], v253 offset:6656
	ds_read_b64_tr_b16 v[238:239], v253 offset:7680
	s_waitcnt lgkmcnt(8)
	v_mfma_f32_32x32x16_bf16 v[50:65], v[168:171], v[156:159], v[50:65]
	v_add_f32_e32 v164, v94, v164
	v_add_f32_e32 v164, v95, v164
	v_add_f32_e32 v164, v96, v164
	v_add_f32_e32 v164, v97, v164
	v_mov_b32_e32 v165, v164
	v_mfma_f32_32x32x16_bf16 v[50:65], v[172:175], v[160:163], v[50:65]
	v_cvt_pk_bf16_f32 v82, v82, v83
	v_cvt_pk_bf16_f32 v83, v84, v85
	v_cvt_pk_bf16_f32 v84, v86, v87
	v_cvt_pk_bf16_f32 v85, v88, v89
	v_cvt_pk_bf16_f32 v86, v90, v91
	v_cvt_pk_bf16_f32 v87, v92, v93
	v_cvt_pk_bf16_f32 v88, v94, v95
	v_cvt_pk_bf16_f32 v89, v96, v97
	v_permlane32_swap_b32_e32 v164, v165
	v_mfma_f32_32x32x16_bf16 v[50:65], v[176:179], v[82:85], v[50:65]
	v_mfma_f32_32x32x16_bf16 v[50:65], v[180:183], v[86:89], v[50:65]
	s_cmp_ge_u32 s13, s30
	s_cbranch_scc1 .Lgqa_b_noload
	s_cmp_lt_u32 s13, s31
	s_cselect_b32 s9, 0, s31
	s_cselect_b32 s35, s12, s29
	s_lshl_b32 s9, s9, 6
	s_sub_i32 s9, s35, s9
	v_add_u32_e32 v118, s9, v137
	v_ashrrev_i32_e32 v119, 31, v118
	v_lshlrev_b64 v[118:119], 8, v[118:119]
	v_lshl_add_u64 v[120:121], v[16:17], 0, v[118:119]
	v_lshl_add_u64 v[122:123], v[134:135], 0, v[118:119]
	global_load_dwordx4 v[118:121], v[120:121], off
	s_nop 0
	global_load_dwordx4 v[122:125], v[122:123], off
.Lgqa_b_ld_done:
	s_waitcnt lgkmcnt(0)
	v_mfma_f32_32x32x16_bf16 v[34:49], v[224:227], v[156:159], v[34:49]
	s_waitcnt vmcnt(2)
	v_add_u32_e32 v252, s11, v187
	ds_write_b128 v252, v[130:133]
	v_add_u32_e32 v252, s11, v214
	ds_write_b128 v252, v[126:129] offset:12288
	v_exp_f32_e32 v143, v98
	v_exp_f32_e32 v145, v99
	v_mfma_f32_32x32x16_bf16 v[34:49], v[228:231], v[160:163], v[34:49]
	v_exp_f32_e32 v141, v100
	v_exp_f32_e32 v144, v101
	v_exp_f32_e32 v139, v102
	v_exp_f32_e32 v142, v103
	v_mfma_f32_32x32x16_bf16 v[34:49], v[232:235], v[82:85], v[34:49]
	v_exp_f32_e32 v138, v104
	v_exp_f32_e32 v140, v105
	v_exp_f32_e32 v151, v106
	v_exp_f32_e32 v153, v107
	v_exp_f32_e32 v149, v108
	v_mfma_f32_32x32x16_bf16 v[34:49], v[236:239], v[86:89], v[34:49]
	v_exp_f32_e32 v152, v109
	v_exp_f32_e32 v147, v110
	v_exp_f32_e32 v150, v111
	v_exp_f32_e32 v146, v112
	v_exp_f32_e32 v148, v113
	v_add_f32_e32 v252, v154, v155
	v_add_f32_e32 v136, v136, v252
	v_add_f32_e32 v252, v164, v165
	v_add_f32_e32 v136, v136, v252
	s_mov_b32 s9, s11
	s_add_i32 s13, s13, 2
	v_add_u32_e32 v137, 0x80, v137
	s_cmp_lt_u32 s8, s0
	s_cbranch_scc0 .Lgqa_exit
	s_mov_b32 s35, s10
	s_mov_b32 s10, s1
	s_branch .LBB0_497
